# code placement: flush head shifted by 4 bytes (pad inside the unexecuted slow-path stub) so step and flush heads both sit at 4 mod 8
# speedup vs baseline: 1.0105x; 1.0105x over previous
.Lslow_cs:
	s_nop 0
	v_add_lshl_u32 v0, s13, v240, 1
	v_ashrrev_i32_e32 v1, 31, v0
	v_lshl_add_u64 v[6:7], v[0:1], 2, v[232:233]
	flat_load_dwordx2 v[0:1], v[6:7]
	s_branch .Lcs_done
